# PLE epilogue hand-pipelined: loads of 3 row groups in flight, into dead fragment / consumed accumulator registers
# baseline (speedup 1.0000x reference)
; #define LAS __attribute__((address_space(3)))
; template <bool FP8>
; __device__ __forceinline__ void epilogue(const Desc& d, const Acc& acc, const Tile& u, LAS unsigned char* lds) {
;     int tz = threadIdx.x; asm volatile("" : "+v"(tz));
;     const int wid = tz >> 6, lane = tz & 63, wr = wid >> 2, wc = wid & 3, fr = lane & 15, fq = lane >> 4;
;     const int lr0 = wr * 64 + fr, lc0 = wc * 32 + 8 * fq;
.LBB0_741:
	v_mov_b32_e32 v2, v0
	s_nop 15
	s_nop 15
	s_movk_i32 s6, 0xffc0
	v_bfe_u32 v26, v2, 6, 2
	v_and_b32_e32 v3, 15, v2
	v_bfe_u32 v27, v2, 4, 2
	v_ashrrev_i32_e32 v2, 2, v2
	v_and_or_b32 v48, v2, s6, v3
	v_lshlrev_b32_e32 v2, 3, v27
	v_lshl_or_b32 v34, v26, 5, v2
	s_cmp_lt_i32 s1, 7
	s_mov_b64 s[6:7], -1
	s_cbranch_scc1 .LBB0_765
	s_cmp_lt_i32 s1, 8
	s_cbranch_scc1 .LBB0_762
	s_cmp_eq_u32 s1, 8
	s_cbranch_scc0 .LBB0_761
	v_lshl_add_u32 v50, s36, 8, v48
	v_ashrrev_i32_e32 v51, 31, v50
	s_lshl_b32 s6, s44, 8
	v_lshlrev_b64 v[52:53], 10, v[50:51]
	s_ashr_i32 s7, s6, 31
	v_lshl_add_u64 v[52:53], v[52:53], 0, s[6:7]
	v_or_b32_e32 v52, v52, v34
	v_lshlrev_b64 v[52:53], 1, v[52:53]
	v_lshl_add_u64 v[58:59], s[50:51], 0, v[52:53]
	v_lshl_add_u64 v[60:61], s[54:55], 0, v[52:53]
	v_lshl_add_u64 v[62:63], s[50:51], 0, v[52:53]
	v_lshlrev_b32_e32 v66, 2, v26
	s_lshl_b32 s6, s44, 2
	s_ashr_i32 s7, s6, 31
	s_lshl_b64 s[6:7], s[6:7], 2
	s_add_u32 s6, s56, s6
	s_addc_u32 s7, s57, s7
	v_lshl_add_u64 v[64:65], s[6:7], 0, v[66:67]
	v_lshlrev_b64 v[52:53], 6, v[50:51]
	v_lshl_add_u64 v[64:65], v[64:65], 0, v[52:53]
	global_load_dwordx4 v[2:5], v[58:59], off
	global_load_dwordx4 v[6:9], v[58:59], off offset:256
	global_load_dwordx4 v[10:13], v[60:61], off
	global_load_dwordx4 v[14:17], v[60:61], off offset:256
	v_add_co_u32_e32 v58, vcc, 0x8000, v58
	s_nop 1
	v_addc_co_u32_e32 v59, vcc, 0, v59, vcc
	v_add_co_u32_e32 v60, vcc, 0x8000, v60
	s_nop 1
	v_addc_co_u32_e32 v61, vcc, 0, v61, vcc
	global_load_dwordx4 v[18:21], v[58:59], off
	global_load_dwordx4 v[22:25], v[58:59], off offset:256
	global_load_dwordx4 v[26:29], v[60:61], off
	global_load_dwordx4 v[30:33], v[60:61], off offset:256
	v_add_co_u32_e32 v58, vcc, 0x8000, v58
	s_nop 1
	v_addc_co_u32_e32 v59, vcc, 0, v59, vcc
	v_add_co_u32_e32 v60, vcc, 0x8000, v60
	s_nop 1
	v_addc_co_u32_e32 v61, vcc, 0, v61, vcc
	global_load_dwordx4 v[34:37], v[58:59], off
	global_load_dwordx4 v[38:41], v[58:59], off offset:256
	global_load_dwordx4 v[42:45], v[60:61], off
	global_load_dwordx4 v[46:49], v[60:61], off offset:256
	v_add_co_u32_e32 v58, vcc, 0x8000, v58
	s_nop 1
	v_addc_co_u32_e32 v59, vcc, 0, v59, vcc
	v_add_co_u32_e32 v60, vcc, 0x8000, v60
	s_nop 1
	v_addc_co_u32_e32 v61, vcc, 0, v61, vcc
	s_waitcnt vmcnt(8)
	v_mul_f32_e32 v72, 0xbfb8aa3b, v72
	v_mul_f32_e32 v73, 0xbfb8aa3b, v73
	v_mul_f32_e32 v74, 0xbfb8aa3b, v74
	v_mul_f32_e32 v75, 0xbfb8aa3b, v75
	v_exp_f32_e32 v72, v72
	v_exp_f32_e32 v73, v73
	v_exp_f32_e32 v74, v74
	v_exp_f32_e32 v75, v75
	v_add_f32_e32 v72, 1.0, v72
	v_add_f32_e32 v73, 1.0, v73
	v_add_f32_e32 v74, 1.0, v74
	v_add_f32_e32 v75, 1.0, v75
	v_rcp_f32_e32 v72, v72
	v_rcp_f32_e32 v73, v73
	v_rcp_f32_e32 v74, v74
	v_rcp_f32_e32 v75, v75
	v_lshlrev_b32_e32 v50, 16, v2
	v_and_b32_e32 v51, 0xffff0000, v2
	v_lshlrev_b32_e32 v52, 16, v3
	v_and_b32_e32 v53, 0xffff0000, v3
	v_lshlrev_b32_e32 v54, 16, v10
	v_and_b32_e32 v55, 0xffff0000, v10
	v_lshlrev_b32_e32 v56, 16, v11
	v_and_b32_e32 v57, 0xffff0000, v11
	v_fmac_f32_e32 v50, v72, v54
	v_fmac_f32_e32 v51, v73, v55
	v_fmac_f32_e32 v52, v74, v56
	v_fmac_f32_e32 v53, v75, v57
	v_cvt_pk_bf16_f32 v2, v50, v51
	v_cvt_pk_bf16_f32 v3, v52, v53
	v_mul_f32_e32 v10, v50, v50
	v_mul_f32_e32 v11, v51, v51
	v_fmac_f32_e32 v10, v52, v52
	v_fmac_f32_e32 v11, v53, v53
	v_mul_f32_e32 v192, 0xbfb8aa3b, v192
	v_mul_f32_e32 v193, 0xbfb8aa3b, v193
	v_mul_f32_e32 v194, 0xbfb8aa3b, v194
	v_mul_f32_e32 v195, 0xbfb8aa3b, v195
	v_exp_f32_e32 v192, v192
	v_exp_f32_e32 v193, v193
	v_exp_f32_e32 v194, v194
	v_exp_f32_e32 v195, v195
	v_add_f32_e32 v192, 1.0, v192
	v_add_f32_e32 v193, 1.0, v193
	v_add_f32_e32 v194, 1.0, v194
	v_add_f32_e32 v195, 1.0, v195
	v_rcp_f32_e32 v192, v192
	v_rcp_f32_e32 v193, v193
	v_rcp_f32_e32 v194, v194
	v_rcp_f32_e32 v195, v195
	v_lshlrev_b32_e32 v50, 16, v4
	v_and_b32_e32 v51, 0xffff0000, v4
	v_lshlrev_b32_e32 v52, 16, v5
	v_and_b32_e32 v53, 0xffff0000, v5
	v_lshlrev_b32_e32 v54, 16, v12
	v_and_b32_e32 v55, 0xffff0000, v12
	v_lshlrev_b32_e32 v56, 16, v13
	v_and_b32_e32 v57, 0xffff0000, v13
	v_fmac_f32_e32 v50, v192, v54
	v_fmac_f32_e32 v51, v193, v55
	v_fmac_f32_e32 v52, v194, v56
	v_fmac_f32_e32 v53, v195, v57
	v_cvt_pk_bf16_f32 v4, v50, v51
	v_cvt_pk_bf16_f32 v5, v52, v53
	v_fmac_f32_e32 v10, v50, v50
	v_fmac_f32_e32 v11, v51, v51
	v_fmac_f32_e32 v10, v52, v52
	v_fmac_f32_e32 v11, v53, v53
	v_mul_f32_e32 v164, 0xbfb8aa3b, v164
	v_mul_f32_e32 v165, 0xbfb8aa3b, v165
	v_mul_f32_e32 v166, 0xbfb8aa3b, v166
	v_mul_f32_e32 v167, 0xbfb8aa3b, v167
	v_exp_f32_e32 v164, v164
	v_exp_f32_e32 v165, v165
	v_exp_f32_e32 v166, v166
	v_exp_f32_e32 v167, v167
	v_add_f32_e32 v164, 1.0, v164
	v_add_f32_e32 v165, 1.0, v165
	v_add_f32_e32 v166, 1.0, v166
	v_add_f32_e32 v167, 1.0, v167
	v_rcp_f32_e32 v164, v164
	v_rcp_f32_e32 v165, v165
	v_rcp_f32_e32 v166, v166
	v_rcp_f32_e32 v167, v167
	v_lshlrev_b32_e32 v50, 16, v6
	v_and_b32_e32 v51, 0xffff0000, v6
	v_lshlrev_b32_e32 v52, 16, v7
	v_and_b32_e32 v53, 0xffff0000, v7
	v_lshlrev_b32_e32 v54, 16, v14
	v_and_b32_e32 v55, 0xffff0000, v14
	v_lshlrev_b32_e32 v56, 16, v15
	v_and_b32_e32 v57, 0xffff0000, v15
	v_fmac_f32_e32 v50, v164, v54
	v_fmac_f32_e32 v51, v165, v55
	v_fmac_f32_e32 v52, v166, v56
	v_fmac_f32_e32 v53, v167, v57
	v_cvt_pk_bf16_f32 v6, v50, v51
	v_cvt_pk_bf16_f32 v7, v52, v53
	v_fmac_f32_e32 v10, v50, v50
	v_fmac_f32_e32 v11, v51, v51
	v_fmac_f32_e32 v10, v52, v52
	v_fmac_f32_e32 v11, v53, v53
	v_mul_f32_e32 v160, 0xbfb8aa3b, v160
	v_mul_f32_e32 v161, 0xbfb8aa3b, v161
	v_mul_f32_e32 v162, 0xbfb8aa3b, v162
	v_mul_f32_e32 v163, 0xbfb8aa3b, v163
	v_exp_f32_e32 v160, v160
	v_exp_f32_e32 v161, v161
	v_exp_f32_e32 v162, v162
	v_exp_f32_e32 v163, v163
	v_add_f32_e32 v160, 1.0, v160
	v_add_f32_e32 v161, 1.0, v161
	v_add_f32_e32 v162, 1.0, v162
	v_add_f32_e32 v163, 1.0, v163
	v_rcp_f32_e32 v160, v160
	v_rcp_f32_e32 v161, v161
	v_rcp_f32_e32 v162, v162
	v_rcp_f32_e32 v163, v163
	v_lshlrev_b32_e32 v50, 16, v8
	v_and_b32_e32 v51, 0xffff0000, v8
	v_lshlrev_b32_e32 v52, 16, v9
	v_and_b32_e32 v53, 0xffff0000, v9
	v_lshlrev_b32_e32 v54, 16, v16
	v_and_b32_e32 v55, 0xffff0000, v16
	v_lshlrev_b32_e32 v56, 16, v17
	v_and_b32_e32 v57, 0xffff0000, v17
	v_fmac_f32_e32 v50, v160, v54
	v_fmac_f32_e32 v51, v161, v55
	v_fmac_f32_e32 v52, v162, v56
	v_fmac_f32_e32 v53, v163, v57
	v_cvt_pk_bf16_f32 v8, v50, v51
	v_cvt_pk_bf16_f32 v9, v52, v53
	v_fmac_f32_e32 v10, v50, v50
	v_fmac_f32_e32 v11, v51, v51
	v_fmac_f32_e32 v10, v52, v52
	v_fmac_f32_e32 v11, v53, v53
	v_add_f32_e32 v10, v10, v11
	global_load_dwordx4 v[72:75], v[58:59], off
	global_load_dwordx4 v[192:195], v[58:59], off offset:256
	global_load_dwordx4 v[164:167], v[60:61], off
	global_load_dwordx4 v[160:163], v[60:61], off offset:256
	v_add_co_u32_e32 v58, vcc, 0x28000, v58
	s_nop 1
	v_addc_co_u32_e32 v59, vcc, 0, v59, vcc
	v_add_co_u32_e32 v60, vcc, 0x28000, v60
	s_nop 1
	v_addc_co_u32_e32 v61, vcc, 0, v61, vcc
	global_store_dwordx4 v[62:63], v[2:5], off
	global_store_dwordx4 v[62:63], v[6:9], off offset:256
	v_add_co_u32_e32 v62, vcc, 0x8000, v62
	s_nop 1
	v_addc_co_u32_e32 v63, vcc, 0, v63, vcc
	s_waitcnt vmcnt(10)
	v_mul_f32_e32 v188, 0xbfb8aa3b, v188
	v_mul_f32_e32 v189, 0xbfb8aa3b, v189
	v_mul_f32_e32 v190, 0xbfb8aa3b, v190
	v_mul_f32_e32 v191, 0xbfb8aa3b, v191
	v_exp_f32_e32 v188, v188
	v_exp_f32_e32 v189, v189
	v_exp_f32_e32 v190, v190
	v_exp_f32_e32 v191, v191
	v_add_f32_e32 v188, 1.0, v188
	v_add_f32_e32 v189, 1.0, v189
	v_add_f32_e32 v190, 1.0, v190
	v_add_f32_e32 v191, 1.0, v191
	v_rcp_f32_e32 v188, v188
	v_rcp_f32_e32 v189, v189
	v_rcp_f32_e32 v190, v190
	v_rcp_f32_e32 v191, v191
	v_lshlrev_b32_e32 v50, 16, v18
	v_and_b32_e32 v51, 0xffff0000, v18
	v_lshlrev_b32_e32 v52, 16, v19
	v_and_b32_e32 v53, 0xffff0000, v19
	v_lshlrev_b32_e32 v54, 16, v26
	v_and_b32_e32 v55, 0xffff0000, v26
	v_lshlrev_b32_e32 v56, 16, v27
	v_and_b32_e32 v57, 0xffff0000, v27
	v_fmac_f32_e32 v50, v188, v54
	v_fmac_f32_e32 v51, v189, v55
	v_fmac_f32_e32 v52, v190, v56
	v_fmac_f32_e32 v53, v191, v57
	v_cvt_pk_bf16_f32 v18, v50, v51
	v_cvt_pk_bf16_f32 v19, v52, v53
	v_mul_f32_e32 v26, v50, v50
	v_mul_f32_e32 v27, v51, v51
	v_fmac_f32_e32 v26, v52, v52
	v_fmac_f32_e32 v27, v53, v53
	v_mul_f32_e32 v184, 0xbfb8aa3b, v184
	v_mul_f32_e32 v185, 0xbfb8aa3b, v185
	v_mul_f32_e32 v186, 0xbfb8aa3b, v186
	v_mul_f32_e32 v187, 0xbfb8aa3b, v187
	v_exp_f32_e32 v184, v184
	v_exp_f32_e32 v185, v185
	v_exp_f32_e32 v186, v186
	v_exp_f32_e32 v187, v187
	v_add_f32_e32 v184, 1.0, v184
	v_add_f32_e32 v185, 1.0, v185
	v_add_f32_e32 v186, 1.0, v186
	v_add_f32_e32 v187, 1.0, v187
	v_rcp_f32_e32 v184, v184
	v_rcp_f32_e32 v185, v185
	v_rcp_f32_e32 v186, v186
	v_rcp_f32_e32 v187, v187
	v_lshlrev_b32_e32 v50, 16, v20
	v_and_b32_e32 v51, 0xffff0000, v20
	v_lshlrev_b32_e32 v52, 16, v21
	v_and_b32_e32 v53, 0xffff0000, v21
	v_lshlrev_b32_e32 v54, 16, v28
	v_and_b32_e32 v55, 0xffff0000, v28
	v_lshlrev_b32_e32 v56, 16, v29
	v_and_b32_e32 v57, 0xffff0000, v29
	v_fmac_f32_e32 v50, v184, v54
	v_fmac_f32_e32 v51, v185, v55
	v_fmac_f32_e32 v52, v186, v56
	v_fmac_f32_e32 v53, v187, v57
	v_cvt_pk_bf16_f32 v20, v50, v51
	v_cvt_pk_bf16_f32 v21, v52, v53
	v_fmac_f32_e32 v26, v50, v50
	v_fmac_f32_e32 v27, v51, v51
	v_fmac_f32_e32 v26, v52, v52
	v_fmac_f32_e32 v27, v53, v53
	v_mul_f32_e32 v156, 0xbfb8aa3b, v156
	v_mul_f32_e32 v157, 0xbfb8aa3b, v157
	v_mul_f32_e32 v158, 0xbfb8aa3b, v158
	v_mul_f32_e32 v159, 0xbfb8aa3b, v159
	v_exp_f32_e32 v156, v156
	v_exp_f32_e32 v157, v157
	v_exp_f32_e32 v158, v158
	v_exp_f32_e32 v159, v159
	v_add_f32_e32 v156, 1.0, v156
	v_add_f32_e32 v157, 1.0, v157
	v_add_f32_e32 v158, 1.0, v158
	v_add_f32_e32 v159, 1.0, v159
	v_rcp_f32_e32 v156, v156
	v_rcp_f32_e32 v157, v157
	v_rcp_f32_e32 v158, v158
	v_rcp_f32_e32 v159, v159
	v_lshlrev_b32_e32 v50, 16, v22
	v_and_b32_e32 v51, 0xffff0000, v22
	v_lshlrev_b32_e32 v52, 16, v23
	v_and_b32_e32 v53, 0xffff0000, v23
	v_lshlrev_b32_e32 v54, 16, v30
	v_and_b32_e32 v55, 0xffff0000, v30
	v_lshlrev_b32_e32 v56, 16, v31
	v_and_b32_e32 v57, 0xffff0000, v31
	v_fmac_f32_e32 v50, v156, v54
	v_fmac_f32_e32 v51, v157, v55
	v_fmac_f32_e32 v52, v158, v56
	v_fmac_f32_e32 v53, v159, v57
	v_cvt_pk_bf16_f32 v22, v50, v51
	v_cvt_pk_bf16_f32 v23, v52, v53
	v_fmac_f32_e32 v26, v50, v50
	v_fmac_f32_e32 v27, v51, v51
	v_fmac_f32_e32 v26, v52, v52
	v_fmac_f32_e32 v27, v53, v53
	v_mul_f32_e32 v152, 0xbfb8aa3b, v152
	v_mul_f32_e32 v153, 0xbfb8aa3b, v153
	v_mul_f32_e32 v154, 0xbfb8aa3b, v154
	v_mul_f32_e32 v155, 0xbfb8aa3b, v155
	v_exp_f32_e32 v152, v152
	v_exp_f32_e32 v153, v153
	v_exp_f32_e32 v154, v154
	v_exp_f32_e32 v155, v155
	v_add_f32_e32 v152, 1.0, v152
	v_add_f32_e32 v153, 1.0, v153
	v_add_f32_e32 v154, 1.0, v154
	v_add_f32_e32 v155, 1.0, v155
	v_rcp_f32_e32 v152, v152
	v_rcp_f32_e32 v153, v153
	v_rcp_f32_e32 v154, v154
	v_rcp_f32_e32 v155, v155
	v_lshlrev_b32_e32 v50, 16, v24
	v_and_b32_e32 v51, 0xffff0000, v24
	v_lshlrev_b32_e32 v52, 16, v25
	v_and_b32_e32 v53, 0xffff0000, v25
	v_lshlrev_b32_e32 v54, 16, v32
	v_and_b32_e32 v55, 0xffff0000, v32
	v_lshlrev_b32_e32 v56, 16, v33
	v_and_b32_e32 v57, 0xffff0000, v33
	v_fmac_f32_e32 v50, v152, v54
	v_fmac_f32_e32 v51, v153, v55
	v_fmac_f32_e32 v52, v154, v56
	v_fmac_f32_e32 v53, v155, v57
	v_cvt_pk_bf16_f32 v24, v50, v51
	v_cvt_pk_bf16_f32 v25, v52, v53
	v_fmac_f32_e32 v26, v50, v50
	v_fmac_f32_e32 v27, v51, v51
	v_fmac_f32_e32 v26, v52, v52
	v_fmac_f32_e32 v27, v53, v53
	v_add_f32_e32 v26, v26, v27
	global_load_dwordx4 v[188:191], v[58:59], off
	global_load_dwordx4 v[184:187], v[58:59], off offset:256
	global_load_dwordx4 v[156:159], v[60:61], off
	global_load_dwordx4 v[152:155], v[60:61], off offset:256
	v_add_co_u32_e32 v58, vcc, 0x8000, v58
	s_nop 1
	v_addc_co_u32_e32 v59, vcc, 0, v59, vcc
	v_add_co_u32_e32 v60, vcc, 0x8000, v60
	s_nop 1
	v_addc_co_u32_e32 v61, vcc, 0, v61, vcc
	global_store_dwordx4 v[62:63], v[18:21], off
	global_store_dwordx4 v[62:63], v[22:25], off offset:256
	v_add_co_u32_e32 v62, vcc, 0x8000, v62
	s_nop 1
	v_addc_co_u32_e32 v63, vcc, 0, v63, vcc
	s_waitcnt vmcnt(12)
	v_mul_f32_e32 v180, 0xbfb8aa3b, v180
	v_mul_f32_e32 v181, 0xbfb8aa3b, v181
	v_mul_f32_e32 v182, 0xbfb8aa3b, v182
	v_mul_f32_e32 v183, 0xbfb8aa3b, v183
	v_exp_f32_e32 v180, v180
	v_exp_f32_e32 v181, v181
	v_exp_f32_e32 v182, v182
	v_exp_f32_e32 v183, v183
	v_add_f32_e32 v180, 1.0, v180
	v_add_f32_e32 v181, 1.0, v181
	v_add_f32_e32 v182, 1.0, v182
	v_add_f32_e32 v183, 1.0, v183
	v_rcp_f32_e32 v180, v180
	v_rcp_f32_e32 v181, v181
	v_rcp_f32_e32 v182, v182
	v_rcp_f32_e32 v183, v183
	v_lshlrev_b32_e32 v50, 16, v34
	v_and_b32_e32 v51, 0xffff0000, v34
	v_lshlrev_b32_e32 v52, 16, v35
	v_and_b32_e32 v53, 0xffff0000, v35
	v_lshlrev_b32_e32 v54, 16, v42
	v_and_b32_e32 v55, 0xffff0000, v42
	v_lshlrev_b32_e32 v56, 16, v43
	v_and_b32_e32 v57, 0xffff0000, v43
	v_fmac_f32_e32 v50, v180, v54
	v_fmac_f32_e32 v51, v181, v55
	v_fmac_f32_e32 v52, v182, v56
	v_fmac_f32_e32 v53, v183, v57
	v_cvt_pk_bf16_f32 v34, v50, v51
	v_cvt_pk_bf16_f32 v35, v52, v53
	v_mul_f32_e32 v42, v50, v50
	v_mul_f32_e32 v43, v51, v51
	v_fmac_f32_e32 v42, v52, v52
	v_fmac_f32_e32 v43, v53, v53
	v_mul_f32_e32 v176, 0xbfb8aa3b, v176
	v_mul_f32_e32 v177, 0xbfb8aa3b, v177
	v_mul_f32_e32 v178, 0xbfb8aa3b, v178
	v_mul_f32_e32 v179, 0xbfb8aa3b, v179
	v_exp_f32_e32 v176, v176
	v_exp_f32_e32 v177, v177
	v_exp_f32_e32 v178, v178
	v_exp_f32_e32 v179, v179
	v_add_f32_e32 v176, 1.0, v176
	v_add_f32_e32 v177, 1.0, v177
	v_add_f32_e32 v178, 1.0, v178
	v_add_f32_e32 v179, 1.0, v179
	v_rcp_f32_e32 v176, v176
	v_rcp_f32_e32 v177, v177
	v_rcp_f32_e32 v178, v178
	v_rcp_f32_e32 v179, v179
	v_lshlrev_b32_e32 v50, 16, v36
	v_and_b32_e32 v51, 0xffff0000, v36
	v_lshlrev_b32_e32 v52, 16, v37
	v_and_b32_e32 v53, 0xffff0000, v37
	v_lshlrev_b32_e32 v54, 16, v44
	v_and_b32_e32 v55, 0xffff0000, v44
	v_lshlrev_b32_e32 v56, 16, v45
	v_and_b32_e32 v57, 0xffff0000, v45
	v_fmac_f32_e32 v50, v176, v54
	v_fmac_f32_e32 v51, v177, v55
	v_fmac_f32_e32 v52, v178, v56
	v_fmac_f32_e32 v53, v179, v57
	v_cvt_pk_bf16_f32 v36, v50, v51
	v_cvt_pk_bf16_f32 v37, v52, v53
	v_fmac_f32_e32 v42, v50, v50
	v_fmac_f32_e32 v43, v51, v51
	v_fmac_f32_e32 v42, v52, v52
	v_fmac_f32_e32 v43, v53, v53
	v_mul_f32_e32 v148, 0xbfb8aa3b, v148
	v_mul_f32_e32 v149, 0xbfb8aa3b, v149
	v_mul_f32_e32 v150, 0xbfb8aa3b, v150
	v_mul_f32_e32 v151, 0xbfb8aa3b, v151
	v_exp_f32_e32 v148, v148
	v_exp_f32_e32 v149, v149
	v_exp_f32_e32 v150, v150
	v_exp_f32_e32 v151, v151
	v_add_f32_e32 v148, 1.0, v148
	v_add_f32_e32 v149, 1.0, v149
	v_add_f32_e32 v150, 1.0, v150
	v_add_f32_e32 v151, 1.0, v151
	v_rcp_f32_e32 v148, v148
	v_rcp_f32_e32 v149, v149
	v_rcp_f32_e32 v150, v150
	v_rcp_f32_e32 v151, v151
	v_lshlrev_b32_e32 v50, 16, v38
	v_and_b32_e32 v51, 0xffff0000, v38
	v_lshlrev_b32_e32 v52, 16, v39
	v_and_b32_e32 v53, 0xffff0000, v39
	v_lshlrev_b32_e32 v54, 16, v46
	v_and_b32_e32 v55, 0xffff0000, v46
	v_lshlrev_b32_e32 v56, 16, v47
	v_and_b32_e32 v57, 0xffff0000, v47
	v_fmac_f32_e32 v50, v148, v54
	v_fmac_f32_e32 v51, v149, v55
	v_fmac_f32_e32 v52, v150, v56
	v_fmac_f32_e32 v53, v151, v57
	v_cvt_pk_bf16_f32 v38, v50, v51
	v_cvt_pk_bf16_f32 v39, v52, v53
	v_fmac_f32_e32 v42, v50, v50
	v_fmac_f32_e32 v43, v51, v51
	v_fmac_f32_e32 v42, v52, v52
	v_fmac_f32_e32 v43, v53, v53
	v_mul_f32_e32 v144, 0xbfb8aa3b, v144
	v_mul_f32_e32 v145, 0xbfb8aa3b, v145
	v_mul_f32_e32 v146, 0xbfb8aa3b, v146
	v_mul_f32_e32 v147, 0xbfb8aa3b, v147
	v_exp_f32_e32 v144, v144
	v_exp_f32_e32 v145, v145
	v_exp_f32_e32 v146, v146
	v_exp_f32_e32 v147, v147
	v_add_f32_e32 v144, 1.0, v144
	v_add_f32_e32 v145, 1.0, v145
	v_add_f32_e32 v146, 1.0, v146
	v_add_f32_e32 v147, 1.0, v147
	v_rcp_f32_e32 v144, v144
	v_rcp_f32_e32 v145, v145
	v_rcp_f32_e32 v146, v146
	v_rcp_f32_e32 v147, v147
	v_lshlrev_b32_e32 v50, 16, v40
	v_and_b32_e32 v51, 0xffff0000, v40
	v_lshlrev_b32_e32 v52, 16, v41
	v_and_b32_e32 v53, 0xffff0000, v41
	v_lshlrev_b32_e32 v54, 16, v48
	v_and_b32_e32 v55, 0xffff0000, v48
	v_lshlrev_b32_e32 v56, 16, v49
	v_and_b32_e32 v57, 0xffff0000, v49
	v_fmac_f32_e32 v50, v144, v54
	v_fmac_f32_e32 v51, v145, v55
	v_fmac_f32_e32 v52, v146, v56
	v_fmac_f32_e32 v53, v147, v57
	v_cvt_pk_bf16_f32 v40, v50, v51
	v_cvt_pk_bf16_f32 v41, v52, v53
	v_fmac_f32_e32 v42, v50, v50
	v_fmac_f32_e32 v43, v51, v51
	v_fmac_f32_e32 v42, v52, v52
	v_fmac_f32_e32 v43, v53, v53
	v_add_f32_e32 v42, v42, v43
	global_load_dwordx4 v[180:183], v[58:59], off
	global_load_dwordx4 v[176:179], v[58:59], off offset:256
	global_load_dwordx4 v[148:151], v[60:61], off
	global_load_dwordx4 v[144:147], v[60:61], off offset:256
	v_add_co_u32_e32 v58, vcc, 0x8000, v58
	s_nop 1
	v_addc_co_u32_e32 v59, vcc, 0, v59, vcc
	v_add_co_u32_e32 v60, vcc, 0x8000, v60
	s_nop 1
	v_addc_co_u32_e32 v61, vcc, 0, v61, vcc
	global_store_dwordx4 v[62:63], v[34:37], off
	global_store_dwordx4 v[62:63], v[38:41], off offset:256
	v_add_co_u32_e32 v62, vcc, 0x8000, v62
	s_nop 1
	v_addc_co_u32_e32 v63, vcc, 0, v63, vcc
	s_waitcnt vmcnt(14)
	v_mul_f32_e32 v172, 0xbfb8aa3b, v172
	v_mul_f32_e32 v173, 0xbfb8aa3b, v173
	v_mul_f32_e32 v174, 0xbfb8aa3b, v174
	v_mul_f32_e32 v175, 0xbfb8aa3b, v175
	v_exp_f32_e32 v172, v172
	v_exp_f32_e32 v173, v173
	v_exp_f32_e32 v174, v174
	v_exp_f32_e32 v175, v175
	v_add_f32_e32 v172, 1.0, v172
	v_add_f32_e32 v173, 1.0, v173
	v_add_f32_e32 v174, 1.0, v174
	v_add_f32_e32 v175, 1.0, v175
	v_rcp_f32_e32 v172, v172
	v_rcp_f32_e32 v173, v173
	v_rcp_f32_e32 v174, v174
	v_rcp_f32_e32 v175, v175
	v_lshlrev_b32_e32 v50, 16, v72
	v_and_b32_e32 v51, 0xffff0000, v72
	v_lshlrev_b32_e32 v52, 16, v73
	v_and_b32_e32 v53, 0xffff0000, v73
	v_lshlrev_b32_e32 v54, 16, v164
	v_and_b32_e32 v55, 0xffff0000, v164
	v_lshlrev_b32_e32 v56, 16, v165
	v_and_b32_e32 v57, 0xffff0000, v165
	v_fmac_f32_e32 v50, v172, v54
	v_fmac_f32_e32 v51, v173, v55
	v_fmac_f32_e32 v52, v174, v56
	v_fmac_f32_e32 v53, v175, v57
	v_cvt_pk_bf16_f32 v72, v50, v51
	v_cvt_pk_bf16_f32 v73, v52, v53
	v_mul_f32_e32 v164, v50, v50
	v_mul_f32_e32 v165, v51, v51
	v_fmac_f32_e32 v164, v52, v52
	v_fmac_f32_e32 v165, v53, v53
	v_mul_f32_e32 v168, 0xbfb8aa3b, v168
	v_mul_f32_e32 v169, 0xbfb8aa3b, v169
	v_mul_f32_e32 v170, 0xbfb8aa3b, v170
	v_mul_f32_e32 v171, 0xbfb8aa3b, v171
	v_exp_f32_e32 v168, v168
	v_exp_f32_e32 v169, v169
	v_exp_f32_e32 v170, v170
	v_exp_f32_e32 v171, v171
	v_add_f32_e32 v168, 1.0, v168
	v_add_f32_e32 v169, 1.0, v169
	v_add_f32_e32 v170, 1.0, v170
	v_add_f32_e32 v171, 1.0, v171
	v_rcp_f32_e32 v168, v168
	v_rcp_f32_e32 v169, v169
	v_rcp_f32_e32 v170, v170
	v_rcp_f32_e32 v171, v171
	v_lshlrev_b32_e32 v50, 16, v74
	v_and_b32_e32 v51, 0xffff0000, v74
	v_lshlrev_b32_e32 v52, 16, v75
	v_and_b32_e32 v53, 0xffff0000, v75
	v_lshlrev_b32_e32 v54, 16, v166
	v_and_b32_e32 v55, 0xffff0000, v166
	v_lshlrev_b32_e32 v56, 16, v167
	v_and_b32_e32 v57, 0xffff0000, v167
	v_fmac_f32_e32 v50, v168, v54
	v_fmac_f32_e32 v51, v169, v55
	v_fmac_f32_e32 v52, v170, v56
	v_fmac_f32_e32 v53, v171, v57
	v_cvt_pk_bf16_f32 v74, v50, v51
	v_cvt_pk_bf16_f32 v75, v52, v53
	v_fmac_f32_e32 v164, v50, v50
	v_fmac_f32_e32 v165, v51, v51
	v_fmac_f32_e32 v164, v52, v52
	v_fmac_f32_e32 v165, v53, v53
	v_mul_f32_e32 v140, 0xbfb8aa3b, v140
	v_mul_f32_e32 v141, 0xbfb8aa3b, v141
	v_mul_f32_e32 v142, 0xbfb8aa3b, v142
	v_mul_f32_e32 v143, 0xbfb8aa3b, v143
	v_exp_f32_e32 v140, v140
	v_exp_f32_e32 v141, v141
	v_exp_f32_e32 v142, v142
	v_exp_f32_e32 v143, v143
	v_add_f32_e32 v140, 1.0, v140
	v_add_f32_e32 v141, 1.0, v141
	v_add_f32_e32 v142, 1.0, v142
	v_add_f32_e32 v143, 1.0, v143
	v_rcp_f32_e32 v140, v140
	v_rcp_f32_e32 v141, v141
	v_rcp_f32_e32 v142, v142
	v_rcp_f32_e32 v143, v143
	v_lshlrev_b32_e32 v50, 16, v192
	v_and_b32_e32 v51, 0xffff0000, v192
	v_lshlrev_b32_e32 v52, 16, v193
	v_and_b32_e32 v53, 0xffff0000, v193
	v_lshlrev_b32_e32 v54, 16, v160
	v_and_b32_e32 v55, 0xffff0000, v160
	v_lshlrev_b32_e32 v56, 16, v161
	v_and_b32_e32 v57, 0xffff0000, v161
	v_fmac_f32_e32 v50, v140, v54
	v_fmac_f32_e32 v51, v141, v55
	v_fmac_f32_e32 v52, v142, v56
	v_fmac_f32_e32 v53, v143, v57
	v_cvt_pk_bf16_f32 v192, v50, v51
	v_cvt_pk_bf16_f32 v193, v52, v53
	v_fmac_f32_e32 v164, v50, v50
	v_fmac_f32_e32 v165, v51, v51
	v_fmac_f32_e32 v164, v52, v52
	v_fmac_f32_e32 v165, v53, v53
	v_mul_f32_e32 v136, 0xbfb8aa3b, v136
	v_mul_f32_e32 v137, 0xbfb8aa3b, v137
	v_mul_f32_e32 v138, 0xbfb8aa3b, v138
	v_mul_f32_e32 v139, 0xbfb8aa3b, v139
	v_exp_f32_e32 v136, v136
	v_exp_f32_e32 v137, v137
	v_exp_f32_e32 v138, v138
	v_exp_f32_e32 v139, v139
	v_add_f32_e32 v136, 1.0, v136
	v_add_f32_e32 v137, 1.0, v137
	v_add_f32_e32 v138, 1.0, v138
	v_add_f32_e32 v139, 1.0, v139
	v_rcp_f32_e32 v136, v136
	v_rcp_f32_e32 v137, v137
	v_rcp_f32_e32 v138, v138
	v_rcp_f32_e32 v139, v139
	v_lshlrev_b32_e32 v50, 16, v194
	v_and_b32_e32 v51, 0xffff0000, v194
	v_lshlrev_b32_e32 v52, 16, v195
	v_and_b32_e32 v53, 0xffff0000, v195
	v_lshlrev_b32_e32 v54, 16, v162
	v_and_b32_e32 v55, 0xffff0000, v162
	v_lshlrev_b32_e32 v56, 16, v163
	v_and_b32_e32 v57, 0xffff0000, v163
	v_fmac_f32_e32 v50, v136, v54
	v_fmac_f32_e32 v51, v137, v55
	v_fmac_f32_e32 v52, v138, v56
	v_fmac_f32_e32 v53, v139, v57
	v_cvt_pk_bf16_f32 v194, v50, v51
	v_cvt_pk_bf16_f32 v195, v52, v53
	v_fmac_f32_e32 v164, v50, v50
	v_fmac_f32_e32 v165, v51, v51
	v_fmac_f32_e32 v164, v52, v52
	v_fmac_f32_e32 v165, v53, v53
	v_add_f32_e32 v164, v164, v165
	global_load_dwordx4 v[172:175], v[58:59], off
	global_load_dwordx4 v[168:171], v[58:59], off offset:256
	global_load_dwordx4 v[140:143], v[60:61], off
	global_load_dwordx4 v[136:139], v[60:61], off offset:256
	v_add_co_u32_e32 v58, vcc, 0x8000, v58
	s_nop 1
	v_addc_co_u32_e32 v59, vcc, 0, v59, vcc
	v_add_co_u32_e32 v60, vcc, 0x8000, v60
	s_nop 1
	v_addc_co_u32_e32 v61, vcc, 0, v61, vcc
	global_store_dwordx4 v[62:63], v[72:75], off
	global_store_dwordx4 v[62:63], v[192:195], off offset:256
	v_add_co_u32_e32 v62, vcc, 0x28000, v62
	s_nop 1
	v_addc_co_u32_e32 v63, vcc, 0, v63, vcc
	s_waitcnt vmcnt(14)
	v_mul_f32_e32 v132, 0xbfb8aa3b, v132
	v_mul_f32_e32 v133, 0xbfb8aa3b, v133
	v_mul_f32_e32 v134, 0xbfb8aa3b, v134
	v_mul_f32_e32 v135, 0xbfb8aa3b, v135
	v_exp_f32_e32 v132, v132
	v_exp_f32_e32 v133, v133
	v_exp_f32_e32 v134, v134
	v_exp_f32_e32 v135, v135
	v_add_f32_e32 v132, 1.0, v132
	v_add_f32_e32 v133, 1.0, v133
	v_add_f32_e32 v134, 1.0, v134
	v_add_f32_e32 v135, 1.0, v135
	v_rcp_f32_e32 v132, v132
	v_rcp_f32_e32 v133, v133
	v_rcp_f32_e32 v134, v134
	v_rcp_f32_e32 v135, v135
	v_lshlrev_b32_e32 v50, 16, v188
	v_and_b32_e32 v51, 0xffff0000, v188
	v_lshlrev_b32_e32 v52, 16, v189
	v_and_b32_e32 v53, 0xffff0000, v189
	v_lshlrev_b32_e32 v54, 16, v156
	v_and_b32_e32 v55, 0xffff0000, v156
	v_lshlrev_b32_e32 v56, 16, v157
	v_and_b32_e32 v57, 0xffff0000, v157
	v_fmac_f32_e32 v50, v132, v54
	v_fmac_f32_e32 v51, v133, v55
	v_fmac_f32_e32 v52, v134, v56
	v_fmac_f32_e32 v53, v135, v57
	v_cvt_pk_bf16_f32 v188, v50, v51
	v_cvt_pk_bf16_f32 v189, v52, v53
	v_mul_f32_e32 v156, v50, v50
	v_mul_f32_e32 v157, v51, v51
	v_fmac_f32_e32 v156, v52, v52
	v_fmac_f32_e32 v157, v53, v53
	v_mul_f32_e32 v128, 0xbfb8aa3b, v128
	v_mul_f32_e32 v129, 0xbfb8aa3b, v129
	v_mul_f32_e32 v130, 0xbfb8aa3b, v130
	v_mul_f32_e32 v131, 0xbfb8aa3b, v131
	v_exp_f32_e32 v128, v128
	v_exp_f32_e32 v129, v129
	v_exp_f32_e32 v130, v130
	v_exp_f32_e32 v131, v131
	v_add_f32_e32 v128, 1.0, v128
	v_add_f32_e32 v129, 1.0, v129
	v_add_f32_e32 v130, 1.0, v130
	v_add_f32_e32 v131, 1.0, v131
	v_rcp_f32_e32 v128, v128
	v_rcp_f32_e32 v129, v129
	v_rcp_f32_e32 v130, v130
	v_rcp_f32_e32 v131, v131
	v_lshlrev_b32_e32 v50, 16, v190
	v_and_b32_e32 v51, 0xffff0000, v190
	v_lshlrev_b32_e32 v52, 16, v191
	v_and_b32_e32 v53, 0xffff0000, v191
	v_lshlrev_b32_e32 v54, 16, v158
	v_and_b32_e32 v55, 0xffff0000, v158
	v_lshlrev_b32_e32 v56, 16, v159
	v_and_b32_e32 v57, 0xffff0000, v159
	v_fmac_f32_e32 v50, v128, v54
	v_fmac_f32_e32 v51, v129, v55
	v_fmac_f32_e32 v52, v130, v56
	v_fmac_f32_e32 v53, v131, v57
	v_cvt_pk_bf16_f32 v190, v50, v51
	v_cvt_pk_bf16_f32 v191, v52, v53
	v_fmac_f32_e32 v156, v50, v50
	v_fmac_f32_e32 v157, v51, v51
	v_fmac_f32_e32 v156, v52, v52
	v_fmac_f32_e32 v157, v53, v53
	v_mul_f32_e32 v100, 0xbfb8aa3b, v100
	v_mul_f32_e32 v101, 0xbfb8aa3b, v101
	v_mul_f32_e32 v102, 0xbfb8aa3b, v102
	v_mul_f32_e32 v103, 0xbfb8aa3b, v103
	v_exp_f32_e32 v100, v100
	v_exp_f32_e32 v101, v101
	v_exp_f32_e32 v102, v102
	v_exp_f32_e32 v103, v103
	v_add_f32_e32 v100, 1.0, v100
	v_add_f32_e32 v101, 1.0, v101
	v_add_f32_e32 v102, 1.0, v102
	v_add_f32_e32 v103, 1.0, v103
	v_rcp_f32_e32 v100, v100
	v_rcp_f32_e32 v101, v101
	v_rcp_f32_e32 v102, v102
	v_rcp_f32_e32 v103, v103
	v_lshlrev_b32_e32 v50, 16, v184
	v_and_b32_e32 v51, 0xffff0000, v184
	v_lshlrev_b32_e32 v52, 16, v185
	v_and_b32_e32 v53, 0xffff0000, v185
	v_lshlrev_b32_e32 v54, 16, v152
	v_and_b32_e32 v55, 0xffff0000, v152
	v_lshlrev_b32_e32 v56, 16, v153
	v_and_b32_e32 v57, 0xffff0000, v153
	v_fmac_f32_e32 v50, v100, v54
	v_fmac_f32_e32 v51, v101, v55
	v_fmac_f32_e32 v52, v102, v56
	v_fmac_f32_e32 v53, v103, v57
	v_cvt_pk_bf16_f32 v184, v50, v51
	v_cvt_pk_bf16_f32 v185, v52, v53
	v_fmac_f32_e32 v156, v50, v50
	v_fmac_f32_e32 v157, v51, v51
	v_fmac_f32_e32 v156, v52, v52
	v_fmac_f32_e32 v157, v53, v53
	v_mul_f32_e32 v96, 0xbfb8aa3b, v96
	v_mul_f32_e32 v97, 0xbfb8aa3b, v97
	v_mul_f32_e32 v98, 0xbfb8aa3b, v98
	v_mul_f32_e32 v99, 0xbfb8aa3b, v99
	v_exp_f32_e32 v96, v96
	v_exp_f32_e32 v97, v97
	v_exp_f32_e32 v98, v98
	v_exp_f32_e32 v99, v99
	v_add_f32_e32 v96, 1.0, v96
	v_add_f32_e32 v97, 1.0, v97
	v_add_f32_e32 v98, 1.0, v98
	v_add_f32_e32 v99, 1.0, v99
	v_rcp_f32_e32 v96, v96
	v_rcp_f32_e32 v97, v97
	v_rcp_f32_e32 v98, v98
	v_rcp_f32_e32 v99, v99
	v_lshlrev_b32_e32 v50, 16, v186
	v_and_b32_e32 v51, 0xffff0000, v186
	v_lshlrev_b32_e32 v52, 16, v187
	v_and_b32_e32 v53, 0xffff0000, v187
	v_lshlrev_b32_e32 v54, 16, v154
	v_and_b32_e32 v55, 0xffff0000, v154
	v_lshlrev_b32_e32 v56, 16, v155
	v_and_b32_e32 v57, 0xffff0000, v155
	v_fmac_f32_e32 v50, v96, v54
	v_fmac_f32_e32 v51, v97, v55
	v_fmac_f32_e32 v52, v98, v56
	v_fmac_f32_e32 v53, v99, v57
	v_cvt_pk_bf16_f32 v186, v50, v51
	v_cvt_pk_bf16_f32 v187, v52, v53
	v_fmac_f32_e32 v156, v50, v50
	v_fmac_f32_e32 v157, v51, v51
	v_fmac_f32_e32 v156, v52, v52
	v_fmac_f32_e32 v157, v53, v53
	v_add_f32_e32 v156, v156, v157
	global_load_dwordx4 v[132:135], v[58:59], off
	global_load_dwordx4 v[128:131], v[58:59], off offset:256
	global_load_dwordx4 v[100:103], v[60:61], off
	global_load_dwordx4 v[96:99], v[60:61], off offset:256
	global_store_dwordx4 v[62:63], v[188:191], off
	global_store_dwordx4 v[62:63], v[184:187], off offset:256
	v_add_co_u32_e32 v62, vcc, 0x8000, v62
	s_nop 1
	v_addc_co_u32_e32 v63, vcc, 0, v63, vcc
	s_waitcnt vmcnt(14)
	v_mul_f32_e32 v124, 0xbfb8aa3b, v124
	v_mul_f32_e32 v125, 0xbfb8aa3b, v125
	v_mul_f32_e32 v126, 0xbfb8aa3b, v126
	v_mul_f32_e32 v127, 0xbfb8aa3b, v127
	v_exp_f32_e32 v124, v124
	v_exp_f32_e32 v125, v125
	v_exp_f32_e32 v126, v126
	v_exp_f32_e32 v127, v127
	v_add_f32_e32 v124, 1.0, v124
	v_add_f32_e32 v125, 1.0, v125
	v_add_f32_e32 v126, 1.0, v126
	v_add_f32_e32 v127, 1.0, v127
	v_rcp_f32_e32 v124, v124
	v_rcp_f32_e32 v125, v125
	v_rcp_f32_e32 v126, v126
	v_rcp_f32_e32 v127, v127
	v_lshlrev_b32_e32 v50, 16, v180
	v_and_b32_e32 v51, 0xffff0000, v180
	v_lshlrev_b32_e32 v52, 16, v181
	v_and_b32_e32 v53, 0xffff0000, v181
	v_lshlrev_b32_e32 v54, 16, v148
	v_and_b32_e32 v55, 0xffff0000, v148
	v_lshlrev_b32_e32 v56, 16, v149
	v_and_b32_e32 v57, 0xffff0000, v149
	v_fmac_f32_e32 v50, v124, v54
	v_fmac_f32_e32 v51, v125, v55
	v_fmac_f32_e32 v52, v126, v56
	v_fmac_f32_e32 v53, v127, v57
	v_cvt_pk_bf16_f32 v180, v50, v51
	v_cvt_pk_bf16_f32 v181, v52, v53
	v_mul_f32_e32 v148, v50, v50
	v_mul_f32_e32 v149, v51, v51
	v_fmac_f32_e32 v148, v52, v52
	v_fmac_f32_e32 v149, v53, v53
	v_mul_f32_e32 v120, 0xbfb8aa3b, v120
	v_mul_f32_e32 v121, 0xbfb8aa3b, v121
	v_mul_f32_e32 v122, 0xbfb8aa3b, v122
	v_mul_f32_e32 v123, 0xbfb8aa3b, v123
	v_exp_f32_e32 v120, v120
	v_exp_f32_e32 v121, v121
	v_exp_f32_e32 v122, v122
	v_exp_f32_e32 v123, v123
	v_add_f32_e32 v120, 1.0, v120
	v_add_f32_e32 v121, 1.0, v121
	v_add_f32_e32 v122, 1.0, v122
	v_add_f32_e32 v123, 1.0, v123
	v_rcp_f32_e32 v120, v120
	v_rcp_f32_e32 v121, v121
	v_rcp_f32_e32 v122, v122
	v_rcp_f32_e32 v123, v123
	v_lshlrev_b32_e32 v50, 16, v182
	v_and_b32_e32 v51, 0xffff0000, v182
	v_lshlrev_b32_e32 v52, 16, v183
	v_and_b32_e32 v53, 0xffff0000, v183
	v_lshlrev_b32_e32 v54, 16, v150
	v_and_b32_e32 v55, 0xffff0000, v150
	v_lshlrev_b32_e32 v56, 16, v151
	v_and_b32_e32 v57, 0xffff0000, v151
	v_fmac_f32_e32 v50, v120, v54
	v_fmac_f32_e32 v51, v121, v55
	v_fmac_f32_e32 v52, v122, v56
	v_fmac_f32_e32 v53, v123, v57
	v_cvt_pk_bf16_f32 v182, v50, v51
	v_cvt_pk_bf16_f32 v183, v52, v53
	v_fmac_f32_e32 v148, v50, v50
	v_fmac_f32_e32 v149, v51, v51
	v_fmac_f32_e32 v148, v52, v52
	v_fmac_f32_e32 v149, v53, v53
	v_mul_f32_e32 v92, 0xbfb8aa3b, v92
	v_mul_f32_e32 v93, 0xbfb8aa3b, v93
	v_mul_f32_e32 v94, 0xbfb8aa3b, v94
	v_mul_f32_e32 v95, 0xbfb8aa3b, v95
	v_exp_f32_e32 v92, v92
	v_exp_f32_e32 v93, v93
	v_exp_f32_e32 v94, v94
	v_exp_f32_e32 v95, v95
	v_add_f32_e32 v92, 1.0, v92
	v_add_f32_e32 v93, 1.0, v93
	v_add_f32_e32 v94, 1.0, v94
	v_add_f32_e32 v95, 1.0, v95
	v_rcp_f32_e32 v92, v92
	v_rcp_f32_e32 v93, v93
	v_rcp_f32_e32 v94, v94
	v_rcp_f32_e32 v95, v95
	v_lshlrev_b32_e32 v50, 16, v176
	v_and_b32_e32 v51, 0xffff0000, v176
	v_lshlrev_b32_e32 v52, 16, v177
	v_and_b32_e32 v53, 0xffff0000, v177
	v_lshlrev_b32_e32 v54, 16, v144
	v_and_b32_e32 v55, 0xffff0000, v144
	v_lshlrev_b32_e32 v56, 16, v145
	v_and_b32_e32 v57, 0xffff0000, v145
	v_fmac_f32_e32 v50, v92, v54
	v_fmac_f32_e32 v51, v93, v55
	v_fmac_f32_e32 v52, v94, v56
	v_fmac_f32_e32 v53, v95, v57
	v_cvt_pk_bf16_f32 v176, v50, v51
	v_cvt_pk_bf16_f32 v177, v52, v53
	v_fmac_f32_e32 v148, v50, v50
	v_fmac_f32_e32 v149, v51, v51
	v_fmac_f32_e32 v148, v52, v52
	v_fmac_f32_e32 v149, v53, v53
	v_mul_f32_e32 v88, 0xbfb8aa3b, v88
	v_mul_f32_e32 v89, 0xbfb8aa3b, v89
	v_mul_f32_e32 v90, 0xbfb8aa3b, v90
	v_mul_f32_e32 v91, 0xbfb8aa3b, v91
	v_exp_f32_e32 v88, v88
	v_exp_f32_e32 v89, v89
	v_exp_f32_e32 v90, v90
	v_exp_f32_e32 v91, v91
	v_add_f32_e32 v88, 1.0, v88
	v_add_f32_e32 v89, 1.0, v89
	v_add_f32_e32 v90, 1.0, v90
	v_add_f32_e32 v91, 1.0, v91
	v_rcp_f32_e32 v88, v88
	v_rcp_f32_e32 v89, v89
	v_rcp_f32_e32 v90, v90
	v_rcp_f32_e32 v91, v91
	v_lshlrev_b32_e32 v50, 16, v178
	v_and_b32_e32 v51, 0xffff0000, v178
	v_lshlrev_b32_e32 v52, 16, v179
	v_and_b32_e32 v53, 0xffff0000, v179
	v_lshlrev_b32_e32 v54, 16, v146
	v_and_b32_e32 v55, 0xffff0000, v146
	v_lshlrev_b32_e32 v56, 16, v147
	v_and_b32_e32 v57, 0xffff0000, v147
	v_fmac_f32_e32 v50, v88, v54
	v_fmac_f32_e32 v51, v89, v55
	v_fmac_f32_e32 v52, v90, v56
	v_fmac_f32_e32 v53, v91, v57
	v_cvt_pk_bf16_f32 v178, v50, v51
	v_cvt_pk_bf16_f32 v179, v52, v53
	v_fmac_f32_e32 v148, v50, v50
	v_fmac_f32_e32 v149, v51, v51
	v_fmac_f32_e32 v148, v52, v52
	v_fmac_f32_e32 v149, v53, v53
	v_add_f32_e32 v148, v148, v149
	global_store_dwordx4 v[62:63], v[180:183], off
	global_store_dwordx4 v[62:63], v[176:179], off offset:256
	v_add_co_u32_e32 v62, vcc, 0x8000, v62
	s_nop 1
	v_addc_co_u32_e32 v63, vcc, 0, v63, vcc
	s_waitcnt vmcnt(10)
	v_mul_f32_e32 v116, 0xbfb8aa3b, v116
	v_mul_f32_e32 v117, 0xbfb8aa3b, v117
	v_mul_f32_e32 v118, 0xbfb8aa3b, v118
	v_mul_f32_e32 v119, 0xbfb8aa3b, v119
	v_exp_f32_e32 v116, v116
	v_exp_f32_e32 v117, v117
	v_exp_f32_e32 v118, v118
	v_exp_f32_e32 v119, v119
	v_add_f32_e32 v116, 1.0, v116
	v_add_f32_e32 v117, 1.0, v117
	v_add_f32_e32 v118, 1.0, v118
	v_add_f32_e32 v119, 1.0, v119
	v_rcp_f32_e32 v116, v116
	v_rcp_f32_e32 v117, v117
	v_rcp_f32_e32 v118, v118
	v_rcp_f32_e32 v119, v119
	v_lshlrev_b32_e32 v50, 16, v172
	v_and_b32_e32 v51, 0xffff0000, v172
	v_lshlrev_b32_e32 v52, 16, v173
	v_and_b32_e32 v53, 0xffff0000, v173
	v_lshlrev_b32_e32 v54, 16, v140
	v_and_b32_e32 v55, 0xffff0000, v140
	v_lshlrev_b32_e32 v56, 16, v141
	v_and_b32_e32 v57, 0xffff0000, v141
	v_fmac_f32_e32 v50, v116, v54
	v_fmac_f32_e32 v51, v117, v55
	v_fmac_f32_e32 v52, v118, v56
	v_fmac_f32_e32 v53, v119, v57
	v_cvt_pk_bf16_f32 v172, v50, v51
	v_cvt_pk_bf16_f32 v173, v52, v53
	v_mul_f32_e32 v140, v50, v50
	v_mul_f32_e32 v141, v51, v51
	v_fmac_f32_e32 v140, v52, v52
	v_fmac_f32_e32 v141, v53, v53
	v_mul_f32_e32 v112, 0xbfb8aa3b, v112
	v_mul_f32_e32 v113, 0xbfb8aa3b, v113
	v_mul_f32_e32 v114, 0xbfb8aa3b, v114
	v_mul_f32_e32 v115, 0xbfb8aa3b, v115
	v_exp_f32_e32 v112, v112
	v_exp_f32_e32 v113, v113
	v_exp_f32_e32 v114, v114
	v_exp_f32_e32 v115, v115
	v_add_f32_e32 v112, 1.0, v112
	v_add_f32_e32 v113, 1.0, v113
	v_add_f32_e32 v114, 1.0, v114
	v_add_f32_e32 v115, 1.0, v115
	v_rcp_f32_e32 v112, v112
	v_rcp_f32_e32 v113, v113
	v_rcp_f32_e32 v114, v114
	v_rcp_f32_e32 v115, v115
	v_lshlrev_b32_e32 v50, 16, v174
	v_and_b32_e32 v51, 0xffff0000, v174
	v_lshlrev_b32_e32 v52, 16, v175
	v_and_b32_e32 v53, 0xffff0000, v175
	v_lshlrev_b32_e32 v54, 16, v142
	v_and_b32_e32 v55, 0xffff0000, v142
	v_lshlrev_b32_e32 v56, 16, v143
	v_and_b32_e32 v57, 0xffff0000, v143
	v_fmac_f32_e32 v50, v112, v54
	v_fmac_f32_e32 v51, v113, v55
	v_fmac_f32_e32 v52, v114, v56
	v_fmac_f32_e32 v53, v115, v57
	v_cvt_pk_bf16_f32 v174, v50, v51
	v_cvt_pk_bf16_f32 v175, v52, v53
	v_fmac_f32_e32 v140, v50, v50
	v_fmac_f32_e32 v141, v51, v51
	v_fmac_f32_e32 v140, v52, v52
	v_fmac_f32_e32 v141, v53, v53
	v_mul_f32_e32 v84, 0xbfb8aa3b, v84
	v_mul_f32_e32 v85, 0xbfb8aa3b, v85
	v_mul_f32_e32 v86, 0xbfb8aa3b, v86
	v_mul_f32_e32 v87, 0xbfb8aa3b, v87
	v_exp_f32_e32 v84, v84
	v_exp_f32_e32 v85, v85
	v_exp_f32_e32 v86, v86
	v_exp_f32_e32 v87, v87
	v_add_f32_e32 v84, 1.0, v84
	v_add_f32_e32 v85, 1.0, v85
	v_add_f32_e32 v86, 1.0, v86
	v_add_f32_e32 v87, 1.0, v87
	v_rcp_f32_e32 v84, v84
	v_rcp_f32_e32 v85, v85
	v_rcp_f32_e32 v86, v86
	v_rcp_f32_e32 v87, v87
	v_lshlrev_b32_e32 v50, 16, v168
	v_and_b32_e32 v51, 0xffff0000, v168
	v_lshlrev_b32_e32 v52, 16, v169
	v_and_b32_e32 v53, 0xffff0000, v169
	v_lshlrev_b32_e32 v54, 16, v136
	v_and_b32_e32 v55, 0xffff0000, v136
	v_lshlrev_b32_e32 v56, 16, v137
	v_and_b32_e32 v57, 0xffff0000, v137
	v_fmac_f32_e32 v50, v84, v54
	v_fmac_f32_e32 v51, v85, v55
	v_fmac_f32_e32 v52, v86, v56
	v_fmac_f32_e32 v53, v87, v57
	v_cvt_pk_bf16_f32 v168, v50, v51
	v_cvt_pk_bf16_f32 v169, v52, v53
	v_fmac_f32_e32 v140, v50, v50
	v_fmac_f32_e32 v141, v51, v51
	v_fmac_f32_e32 v140, v52, v52
	v_fmac_f32_e32 v141, v53, v53
	v_mul_f32_e32 v80, 0xbfb8aa3b, v80
	v_mul_f32_e32 v81, 0xbfb8aa3b, v81
	v_mul_f32_e32 v82, 0xbfb8aa3b, v82
	v_mul_f32_e32 v83, 0xbfb8aa3b, v83
	v_exp_f32_e32 v80, v80
	v_exp_f32_e32 v81, v81
	v_exp_f32_e32 v82, v82
	v_exp_f32_e32 v83, v83
	v_add_f32_e32 v80, 1.0, v80
	v_add_f32_e32 v81, 1.0, v81
	v_add_f32_e32 v82, 1.0, v82
	v_add_f32_e32 v83, 1.0, v83
	v_rcp_f32_e32 v80, v80
	v_rcp_f32_e32 v81, v81
	v_rcp_f32_e32 v82, v82
	v_rcp_f32_e32 v83, v83
	v_lshlrev_b32_e32 v50, 16, v170
	v_and_b32_e32 v51, 0xffff0000, v170
	v_lshlrev_b32_e32 v52, 16, v171
	v_and_b32_e32 v53, 0xffff0000, v171
	v_lshlrev_b32_e32 v54, 16, v138
	v_and_b32_e32 v55, 0xffff0000, v138
	v_lshlrev_b32_e32 v56, 16, v139
	v_and_b32_e32 v57, 0xffff0000, v139
	v_fmac_f32_e32 v50, v80, v54
	v_fmac_f32_e32 v51, v81, v55
	v_fmac_f32_e32 v52, v82, v56
	v_fmac_f32_e32 v53, v83, v57
	v_cvt_pk_bf16_f32 v170, v50, v51
	v_cvt_pk_bf16_f32 v171, v52, v53
	v_fmac_f32_e32 v140, v50, v50
	v_fmac_f32_e32 v141, v51, v51
	v_fmac_f32_e32 v140, v52, v52
	v_fmac_f32_e32 v141, v53, v53
	v_add_f32_e32 v140, v140, v141
	global_store_dwordx4 v[62:63], v[172:175], off
	global_store_dwordx4 v[62:63], v[168:171], off offset:256
	v_add_co_u32_e32 v62, vcc, 0x8000, v62
	s_nop 1
	v_addc_co_u32_e32 v63, vcc, 0, v63, vcc
	s_waitcnt vmcnt(6)
	v_mul_f32_e32 v108, 0xbfb8aa3b, v108
	v_mul_f32_e32 v109, 0xbfb8aa3b, v109
	v_mul_f32_e32 v110, 0xbfb8aa3b, v110
	v_mul_f32_e32 v111, 0xbfb8aa3b, v111
	v_exp_f32_e32 v108, v108
	v_exp_f32_e32 v109, v109
	v_exp_f32_e32 v110, v110
	v_exp_f32_e32 v111, v111
	v_add_f32_e32 v108, 1.0, v108
	v_add_f32_e32 v109, 1.0, v109
	v_add_f32_e32 v110, 1.0, v110
	v_add_f32_e32 v111, 1.0, v111
	v_rcp_f32_e32 v108, v108
	v_rcp_f32_e32 v109, v109
	v_rcp_f32_e32 v110, v110
	v_rcp_f32_e32 v111, v111
	v_lshlrev_b32_e32 v50, 16, v132
	v_and_b32_e32 v51, 0xffff0000, v132
	v_lshlrev_b32_e32 v52, 16, v133
	v_and_b32_e32 v53, 0xffff0000, v133
	v_lshlrev_b32_e32 v54, 16, v100
	v_and_b32_e32 v55, 0xffff0000, v100
	v_lshlrev_b32_e32 v56, 16, v101
	v_and_b32_e32 v57, 0xffff0000, v101
	v_fmac_f32_e32 v50, v108, v54
	v_fmac_f32_e32 v51, v109, v55
	v_fmac_f32_e32 v52, v110, v56
	v_fmac_f32_e32 v53, v111, v57
	v_cvt_pk_bf16_f32 v132, v50, v51
	v_cvt_pk_bf16_f32 v133, v52, v53
	v_mul_f32_e32 v100, v50, v50
	v_mul_f32_e32 v101, v51, v51
	v_fmac_f32_e32 v100, v52, v52
	v_fmac_f32_e32 v101, v53, v53
	v_mul_f32_e32 v104, 0xbfb8aa3b, v104
	v_mul_f32_e32 v105, 0xbfb8aa3b, v105
	v_mul_f32_e32 v106, 0xbfb8aa3b, v106
	v_mul_f32_e32 v107, 0xbfb8aa3b, v107
	v_exp_f32_e32 v104, v104
	v_exp_f32_e32 v105, v105
	v_exp_f32_e32 v106, v106
	v_exp_f32_e32 v107, v107
	v_add_f32_e32 v104, 1.0, v104
	v_add_f32_e32 v105, 1.0, v105
	v_add_f32_e32 v106, 1.0, v106
	v_add_f32_e32 v107, 1.0, v107
	v_rcp_f32_e32 v104, v104
	v_rcp_f32_e32 v105, v105
	v_rcp_f32_e32 v106, v106
	v_rcp_f32_e32 v107, v107
	v_lshlrev_b32_e32 v50, 16, v134
	v_and_b32_e32 v51, 0xffff0000, v134
	v_lshlrev_b32_e32 v52, 16, v135
	v_and_b32_e32 v53, 0xffff0000, v135
	v_lshlrev_b32_e32 v54, 16, v102
	v_and_b32_e32 v55, 0xffff0000, v102
	v_lshlrev_b32_e32 v56, 16, v103
	v_and_b32_e32 v57, 0xffff0000, v103
	v_fmac_f32_e32 v50, v104, v54
	v_fmac_f32_e32 v51, v105, v55
	v_fmac_f32_e32 v52, v106, v56
	v_fmac_f32_e32 v53, v107, v57
	v_cvt_pk_bf16_f32 v134, v50, v51
	v_cvt_pk_bf16_f32 v135, v52, v53
	v_fmac_f32_e32 v100, v50, v50
	v_fmac_f32_e32 v101, v51, v51
	v_fmac_f32_e32 v100, v52, v52
	v_fmac_f32_e32 v101, v53, v53
	v_mul_f32_e32 v76, 0xbfb8aa3b, v76
	v_mul_f32_e32 v77, 0xbfb8aa3b, v77
	v_mul_f32_e32 v78, 0xbfb8aa3b, v78
	v_mul_f32_e32 v79, 0xbfb8aa3b, v79
	v_exp_f32_e32 v76, v76
	v_exp_f32_e32 v77, v77
	v_exp_f32_e32 v78, v78
	v_exp_f32_e32 v79, v79
	v_add_f32_e32 v76, 1.0, v76
	v_add_f32_e32 v77, 1.0, v77
	v_add_f32_e32 v78, 1.0, v78
	v_add_f32_e32 v79, 1.0, v79
	v_rcp_f32_e32 v76, v76
	v_rcp_f32_e32 v77, v77
	v_rcp_f32_e32 v78, v78
	v_rcp_f32_e32 v79, v79
	v_lshlrev_b32_e32 v50, 16, v128
	v_and_b32_e32 v51, 0xffff0000, v128
	v_lshlrev_b32_e32 v52, 16, v129
	v_and_b32_e32 v53, 0xffff0000, v129
	v_lshlrev_b32_e32 v54, 16, v96
	v_and_b32_e32 v55, 0xffff0000, v96
	v_lshlrev_b32_e32 v56, 16, v97
	v_and_b32_e32 v57, 0xffff0000, v97
	v_fmac_f32_e32 v50, v76, v54
	v_fmac_f32_e32 v51, v77, v55
	v_fmac_f32_e32 v52, v78, v56
	v_fmac_f32_e32 v53, v79, v57
	v_cvt_pk_bf16_f32 v128, v50, v51
	v_cvt_pk_bf16_f32 v129, v52, v53
	v_fmac_f32_e32 v100, v50, v50
	v_fmac_f32_e32 v101, v51, v51
	v_fmac_f32_e32 v100, v52, v52
	v_fmac_f32_e32 v101, v53, v53
	v_mul_f32_e32 v68, 0xbfb8aa3b, v68
	v_mul_f32_e32 v69, 0xbfb8aa3b, v69
	v_mul_f32_e32 v70, 0xbfb8aa3b, v70
	v_mul_f32_e32 v71, 0xbfb8aa3b, v71
	v_exp_f32_e32 v68, v68
	v_exp_f32_e32 v69, v69
	v_exp_f32_e32 v70, v70
	v_exp_f32_e32 v71, v71
	v_add_f32_e32 v68, 1.0, v68
	v_add_f32_e32 v69, 1.0, v69
	v_add_f32_e32 v70, 1.0, v70
	v_add_f32_e32 v71, 1.0, v71
	v_rcp_f32_e32 v68, v68
	v_rcp_f32_e32 v69, v69
	v_rcp_f32_e32 v70, v70
	v_rcp_f32_e32 v71, v71
	v_lshlrev_b32_e32 v50, 16, v130
	v_and_b32_e32 v51, 0xffff0000, v130
	v_lshlrev_b32_e32 v52, 16, v131
	v_and_b32_e32 v53, 0xffff0000, v131
	v_lshlrev_b32_e32 v54, 16, v98
	v_and_b32_e32 v55, 0xffff0000, v98
	v_lshlrev_b32_e32 v56, 16, v99
	v_and_b32_e32 v57, 0xffff0000, v99
	v_fmac_f32_e32 v50, v68, v54
	v_fmac_f32_e32 v51, v69, v55
	v_fmac_f32_e32 v52, v70, v56
	v_fmac_f32_e32 v53, v71, v57
	v_cvt_pk_bf16_f32 v130, v50, v51
	v_cvt_pk_bf16_f32 v131, v52, v53
	v_fmac_f32_e32 v100, v50, v50
	v_fmac_f32_e32 v101, v51, v51
	v_fmac_f32_e32 v100, v52, v52
	v_fmac_f32_e32 v101, v53, v53
	v_add_f32_e32 v100, v100, v101
	global_store_dwordx4 v[62:63], v[132:135], off
	global_store_dwordx4 v[62:63], v[128:131], off offset:256
	v_xor_b32_e32 v108, 16, v238
	v_xor_b32_e32 v109, 32, v238
	v_lshlrev_b32_e32 v108, 2, v108
	v_lshlrev_b32_e32 v109, 2, v109
	ds_bpermute_b32 v50, v108, v10
	ds_bpermute_b32 v51, v108, v26
	ds_bpermute_b32 v52, v108, v42
	ds_bpermute_b32 v53, v108, v164
	ds_bpermute_b32 v54, v108, v156
	ds_bpermute_b32 v55, v108, v148
	ds_bpermute_b32 v56, v108, v140
	ds_bpermute_b32 v57, v108, v100
	s_waitcnt lgkmcnt(0)
	v_add_f32_e32 v10, v10, v50
	v_add_f32_e32 v26, v26, v51
	v_add_f32_e32 v42, v42, v52
	v_add_f32_e32 v164, v164, v53
	v_add_f32_e32 v156, v156, v54
	v_add_f32_e32 v148, v148, v55
	v_add_f32_e32 v140, v140, v56
	v_add_f32_e32 v100, v100, v57
	ds_bpermute_b32 v50, v109, v10
	ds_bpermute_b32 v51, v109, v26
	ds_bpermute_b32 v52, v109, v42
	ds_bpermute_b32 v53, v109, v164
	ds_bpermute_b32 v54, v109, v156
	ds_bpermute_b32 v55, v109, v148
	ds_bpermute_b32 v56, v109, v140
	ds_bpermute_b32 v57, v109, v100
	s_waitcnt lgkmcnt(0)
	v_add_f32_e32 v10, v10, v50
	v_add_f32_e32 v26, v26, v51
	v_add_f32_e32 v42, v42, v52
	v_add_f32_e32 v164, v164, v53
	v_add_f32_e32 v156, v156, v54
	v_add_f32_e32 v148, v148, v55
	v_add_f32_e32 v140, v140, v56
	v_add_f32_e32 v100, v100, v57
	s_mov_b64 s[6:7], exec
	s_mov_b64 exec, 0xffff
	global_store_dword v[64:65], v10, off
	global_store_dword v[64:65], v26, off offset:1024
	global_store_dword v[64:65], v42, off offset:2048
	global_store_dword v[64:65], v164, off offset:3072
	v_add_co_u32_e32 v64, vcc, 0x2000, v64
	s_nop 1
	v_addc_co_u32_e32 v65, vcc, 0, v65, vcc
	global_store_dword v[64:65], v156, off
	global_store_dword v[64:65], v148, off offset:1024
	global_store_dword v[64:65], v140, off offset:2048
	global_store_dword v[64:65], v100, off offset:3072
	s_mov_b64 exec, s[6:7]
